# DSA masked attention tile loop: hoisted and batched K/bias/mask/V LDS reads with counted lgkmcnt, extra VGPRs from dead top-k key registers
# speedup vs baseline: 1.0125x; 1.0125x over previous
.LBB0_1634:
	v_pk_add_f32 v[36:37], v[36:37], v[90:91] op_sel_hi:[1,0] neg_lo:[0,1] neg_hi:[0,1]
	v_pk_add_f32 v[38:39], v[38:39], v[90:91] op_sel_hi:[1,0] neg_lo:[0,1] neg_hi:[0,1]
	v_exp_f32_e32 v36, v36
	v_exp_f32_e32 v37, v37
	v_exp_f32_e32 v38, v38
	v_exp_f32_e32 v39, v39
	v_pk_add_f32 v[40:41], v[40:41], v[90:91] op_sel_hi:[1,0] neg_lo:[0,1] neg_hi:[0,1]
	v_pk_add_f32 v[42:43], v[42:43], v[90:91] op_sel_hi:[1,0] neg_lo:[0,1] neg_hi:[0,1]
	v_exp_f32_e32 v40, v40
	v_exp_f32_e32 v41, v41
	v_exp_f32_e32 v42, v42
	v_exp_f32_e32 v43, v43
	v_pk_add_f32 v[44:45], v[44:45], v[90:91] op_sel_hi:[1,0] neg_lo:[0,1] neg_hi:[0,1]
	v_pk_add_f32 v[114:115], v[36:37], 0 op_sel_hi:[1,0]
	v_exp_f32_e32 v44, v44
	v_exp_f32_e32 v45, v45
	v_pk_add_f32 v[46:47], v[46:47], v[90:91] op_sel_hi:[1,0] neg_lo:[0,1] neg_hi:[0,1]
	v_pk_add_f32 v[114:115], v[38:39], v[114:115]
	v_exp_f32_e32 v46, v46
	v_exp_f32_e32 v47, v47
	v_pk_add_f32 v[48:49], v[48:49], v[90:91] op_sel_hi:[1,0] neg_lo:[0,1] neg_hi:[0,1]
	v_pk_add_f32 v[114:115], v[40:41], v[114:115]
	v_exp_f32_e32 v48, v48
	v_exp_f32_e32 v49, v49
	v_pk_add_f32 v[50:51], v[50:51], v[90:91] op_sel_hi:[1,0] neg_lo:[0,1] neg_hi:[0,1]
	v_pk_add_f32 v[114:115], v[42:43], v[114:115]
	v_exp_f32_e32 v50, v50
	v_exp_f32_e32 v51, v51
	v_pk_add_f32 v[114:115], v[44:45], v[114:115]
	v_cvt_pk_bf16_f32 v36, v36, v37
	v_pk_add_f32 v[114:115], v[46:47], v[114:115]
	v_cvt_pk_bf16_f32 v37, v38, v39
	v_pk_add_f32 v[114:115], v[48:49], v[114:115]
	v_cvt_pk_bf16_f32 v38, v40, v41
	v_pk_add_f32 v[114:115], v[50:51], v[114:115]
	v_cvt_pk_bf16_f32 v39, v42, v43
	v_cvt_pk_bf16_f32 v40, v44, v45
	v_cvt_pk_bf16_f32 v41, v46, v47
	v_cvt_pk_bf16_f32 v42, v48, v49
	v_cvt_pk_bf16_f32 v43, v50, v51
	v_add_f32_e32 v2, v114, v115
	s_setprio 1
	v_add_f32_e32 v110, v110, v2
	s_waitcnt lgkmcnt(0)
	v_mfma_f32_32x32x16_bf16 v[20:35], v[156:159], v[36:39], v[20:35]
	v_mfma_f32_32x32x16_bf16 v[4:19], v[162:165], v[36:39], v[4:19]
	v_mfma_f32_32x32x16_bf16 v[20:35], v[166:169], v[40:43], v[20:35]
	v_mfma_f32_32x32x16_bf16 v[4:19], v[170:173], v[40:43], v[4:19]
	s_setprio 0

.LBB0_1654:
	s_or_b64 exec, exec, s[8:9]
	v_cmp_le_u32_e32 vcc, s17, v97
	s_and_saveexec_b64 s[8:9], vcc
	s_cbranch_execz .LBB0_1635
	s_lshl_b32 s10, s16, 14
	s_setprio 1
	v_add3_u32 v2, s10, v93, v92
	v_add3_u32 v174, s10, v94, v92
	v_add3_u32 v175, s10, v95, v92
	v_add3_u32 v176, s10, v96, v92
	ds_read_b128 v[36:39], v2 offset:50048
	ds_read_b128 v[114:117], v174 offset:50048
	ds_read_b128 v[132:135], v175 offset:50048
	ds_read_b128 v[136:139], v176 offset:50048
	ds_read_b32 v177, v112
	ds_read2_b32 v[140:141], v113 offset0:26 offset1:27
	ds_read2_b32 v[142:143], v113 offset0:24 offset1:25
	ds_read2_b32 v[144:145], v113 offset0:18 offset1:19
	ds_read2_b32 v[146:147], v113 offset0:16 offset1:17
	ds_read2_b32 v[148:149], v113 offset0:10 offset1:11
	ds_read2_b32 v[150:151], v113 offset0:8 offset1:9
	ds_read2_b32 v[152:153], v113 offset0:2 offset1:3
	ds_read2_b32 v[154:155], v113 offset1:1
	s_waitcnt lgkmcnt(12)
	v_mfma_f32_32x32x16_bf16 v[36:51], v[36:39], v[52:55], 0
	s_waitcnt lgkmcnt(11)
	v_mfma_f32_32x32x16_bf16 v[36:51], v[114:117], v[56:59], v[36:51]
	s_waitcnt lgkmcnt(10)
	v_mfma_f32_32x32x16_bf16 v[36:51], v[132:135], v[60:63], v[36:51]
	s_waitcnt lgkmcnt(9)
	v_mfma_f32_32x32x16_bf16 v[36:51], v[136:139], v[64:67], v[36:51]
	s_setprio 0
	v_add3_u32 v174, s10, v98, v107
	v_add3_u32 v175, s10, v99, v107
	ds_read_b128 v[156:159], v174 offset:58240
	ds_read_b128 v[162:165], v174 offset:60288
	ds_read_b128 v[166:169], v175 offset:58240
	ds_read_b128 v[170:173], v175 offset:60288
	s_waitcnt lgkmcnt(4)
	v_lshrrev_b32_e32 v2, v102, v177
	s_nop 3
	v_pk_fma_f32 v[36:37], v[36:37], s[82:83], v[140:141] op_sel:[0,0,1] op_sel_hi:[1,0,0]
	v_and_b32_e32 v114, 1, v2
	v_cmp_eq_u32_e32 vcc, 1, v114
	v_and_b32_e32 v114, 2, v2
	s_nop 0
	v_cndmask_b32_e32 v36, v228, v36, vcc
	v_cmp_ne_u32_e32 vcc, 0, v114
	v_pk_fma_f32 v[38:39], v[38:39], s[82:83], v[142:143] op_sel:[0,0,1] op_sel_hi:[1,0,0]
	v_and_b32_e32 v114, 4, v2
	v_cndmask_b32_e32 v37, v228, v37, vcc
	v_cmp_ne_u32_e32 vcc, 0, v114
	v_and_b32_e32 v114, 8, v2
	v_max_f32_e32 v116, v36, v37
	v_cndmask_b32_e32 v38, v228, v38, vcc
	v_cmp_ne_u32_e32 vcc, 0, v114
	s_nop 1
	v_cndmask_b32_e32 v39, v228, v39, vcc
	v_max_f32_e32 v114, v38, v39
	v_max3_f32 v116, v116, s90, v114
	v_pk_fma_f32 v[40:41], v[40:41], s[82:83], v[144:145] op_sel:[0,0,1] op_sel_hi:[1,0,0]
	v_and_b32_e32 v114, 0x100, v2
	v_cmp_ne_u32_e32 vcc, 0, v114
	v_and_b32_e32 v114, 0x200, v2
	s_nop 0
	v_cndmask_b32_e32 v40, v228, v40, vcc
	v_cmp_ne_u32_e32 vcc, 0, v114
	v_pk_fma_f32 v[42:43], v[42:43], s[82:83], v[146:147] op_sel:[0,0,1] op_sel_hi:[1,0,0]
	v_and_b32_e32 v114, 0x400, v2
	v_cndmask_b32_e32 v41, v228, v41, vcc
	v_cmp_ne_u32_e32 vcc, 0, v114
	v_and_b32_e32 v114, 0x800, v2
	v_max_f32_e32 v117, v40, v41
	v_cndmask_b32_e32 v42, v228, v42, vcc
	v_cmp_ne_u32_e32 vcc, 0, v114
	s_nop 1
	v_cndmask_b32_e32 v43, v228, v43, vcc
	v_max_f32_e32 v114, v42, v43
	v_max3_f32 v116, v116, v117, v114
	v_pk_fma_f32 v[44:45], v[44:45], s[82:83], v[148:149] op_sel:[0,0,1] op_sel_hi:[1,0,0]
	v_and_b32_e32 v114, 0x10000, v2
	v_cmp_ne_u32_e32 vcc, 0, v114
	v_and_b32_e32 v114, 0x20000, v2
	s_nop 0
	v_cndmask_b32_e32 v44, v228, v44, vcc
	v_cmp_ne_u32_e32 vcc, 0, v114
	v_pk_fma_f32 v[46:47], v[46:47], s[82:83], v[150:151] op_sel:[0,0,1] op_sel_hi:[1,0,0]
	v_and_b32_e32 v114, 0x40000, v2
	v_cndmask_b32_e32 v45, v228, v45, vcc
	v_cmp_ne_u32_e32 vcc, 0, v114
	v_and_b32_e32 v114, 0x80000, v2
	v_max_f32_e32 v117, v44, v45
	v_cndmask_b32_e32 v46, v228, v46, vcc
	v_cmp_ne_u32_e32 vcc, 0, v114
	s_nop 1
	v_cndmask_b32_e32 v47, v228, v47, vcc
	v_max_f32_e32 v114, v46, v47
	v_max3_f32 v116, v116, v117, v114
	v_pk_fma_f32 v[48:49], v[48:49], s[82:83], v[152:153] op_sel:[0,0,1] op_sel_hi:[1,0,0]
	v_and_b32_e32 v114, 0x1000000, v2
	v_cmp_ne_u32_e32 vcc, 0, v114
	v_and_b32_e32 v114, 0x2000000, v2
	s_nop 0
	v_cndmask_b32_e32 v48, v228, v48, vcc
	v_cmp_ne_u32_e32 vcc, 0, v114
	v_pk_fma_f32 v[50:51], v[50:51], s[82:83], v[154:155] op_sel:[0,0,1] op_sel_hi:[1,0,0]
	v_and_b32_e32 v114, 0x4000000, v2
	v_cndmask_b32_e32 v49, v228, v49, vcc
	v_cmp_ne_u32_e32 vcc, 0, v114
	v_and_b32_e32 v2, 0x8000000, v2
	v_and_b32_e32 v115, 64, v214
	v_cndmask_b32_e32 v50, v228, v50, vcc
	v_cmp_ne_u32_e32 vcc, 0, v2
	v_xor_b32_e32 v114, 32, v214
	v_add_u32_e32 v115, 64, v115
	v_cndmask_b32_e32 v51, v228, v51, vcc
	v_cmp_lt_i32_e32 vcc, v114, v115
	v_max_f32_e32 v117, v48, v49
	v_max_f32_e32 v2, v50, v51
	v_cndmask_b32_e32 v114, v214, v114, vcc
	v_max3_f32 v2, v116, v117, v2
	v_lshlrev_b32_e32 v114, 2, v114
	ds_bpermute_b32 v114, v114, v2
	s_waitcnt lgkmcnt(0)
	v_max_f32_e32 v114, v114, v114
	v_max_f32_e32 v2, v2, v114
	v_add_f32_e32 v114, 0x41000000, v90
	v_cmp_gt_f32_e32 vcc, v2, v114
	s_cbranch_vccz .LBB0_1634
	v_max_f32_e32 v2, v2, v2
	v_max_f32_e32 v114, v90, v90
	v_max_f32_e32 v114, v114, v2
	v_sub_f32_e32 v2, v90, v114
	v_exp_f32_e32 v2, v2
	v_mov_b32_e32 v90, v114
	v_pk_mul_f32 v[34:35], v[34:35], v[2:3] op_sel_hi:[1,0]
	v_pk_mul_f32 v[32:33], v[32:33], v[2:3] op_sel_hi:[1,0]
	v_pk_mul_f32 v[30:31], v[30:31], v[2:3] op_sel_hi:[1,0]
	v_pk_mul_f32 v[28:29], v[28:29], v[2:3] op_sel_hi:[1,0]
	v_pk_mul_f32 v[26:27], v[26:27], v[2:3] op_sel_hi:[1,0]
	v_pk_mul_f32 v[24:25], v[24:25], v[2:3] op_sel_hi:[1,0]
	v_pk_mul_f32 v[22:23], v[22:23], v[2:3] op_sel_hi:[1,0]
	v_pk_mul_f32 v[20:21], v[20:21], v[2:3] op_sel_hi:[1,0]
	v_pk_mul_f32 v[18:19], v[18:19], v[2:3] op_sel_hi:[1,0]
	v_pk_mul_f32 v[16:17], v[16:17], v[2:3] op_sel_hi:[1,0]
	v_pk_mul_f32 v[14:15], v[14:15], v[2:3] op_sel_hi:[1,0]
	v_pk_mul_f32 v[12:13], v[12:13], v[2:3] op_sel_hi:[1,0]
	v_pk_mul_f32 v[10:11], v[10:11], v[2:3] op_sel_hi:[1,0]
	v_pk_mul_f32 v[8:9], v[8:9], v[2:3] op_sel_hi:[1,0]
	v_pk_mul_f32 v[6:7], v[6:7], v[2:3] op_sel_hi:[1,0]
	v_pk_mul_f32 v[4:5], v[4:5], v[2:3] op_sel_hi:[1,0]
	v_mul_f32_e32 v110, v110, v2
	s_branch .LBB0_1634
